# u14 + the second half's whole finishSM (deferred exps, row sums, bf16 packing) executed before the mid-iteration barrier
# baseline (speedup 1.0000x reference)
; #define PK4(P, BASE, OUT) do { u32x4 w = {cvt_pk_bf16(P[BASE + 0], P[BASE + 1]), cvt_pk_bf16(P[BASE + 2], P[BASE + 3]), cvt_pk_bf16(P[BASE + 4], P[BASE + 5]), cvt_pk_bf16(P[BASE + 6], P[BASE + 7])}; \
;     OUT = *reinterpret_cast<bf16x8*>(&w); } while (0)
; DEVI void finishSM(f32x16& p0, f32x16& p1, float alpha, float& l_reg, bf16x8& pa0, bf16x8& pa1, bf16x8& pa2, bf16x8& pa3) {
; #pragma unroll
;     for (int r = 0; r < 16; ++r) p1[r] = __builtin_amdgcn_exp2f(p1[r]);
;     f32x2 s2 = (f32x2){p0[0], p0[1]} + (f32x2){p1[0], p1[1]};
; #pragma unroll
;     for (int r = 2; r < 16; r += 2) s2 += (f32x2){p0[r], p0[r + 1]} + (f32x2){p1[r], p1[r + 1]};
;     float ps = s2[0] + s2[1];
;     { auto rr = __builtin_amdgcn_permlane32_swap(__float_as_uint(ps), __float_as_uint(ps), false, false);
;       ps = __uint_as_float(rr[0]) + __uint_as_float(rr[1]); }
;     l_reg = l_reg * alpha + ps;
;     ...
;     PK4(p0, 0, pa0); PK4(p0, 8, pa1); PK4(p1, 0, pa2); PK4(p1, 8, pa3);
;     ...
; }
.LBB0_699:
	v_exp_f32_e32 v82, v82
	v_exp_f32_e32 v83, v83
	v_exp_f32_e32 v84, v84
	v_exp_f32_e32 v85, v85
	v_exp_f32_e32 v86, v86
	v_exp_f32_e32 v87, v87
	v_exp_f32_e32 v88, v88
	v_exp_f32_e32 v89, v89
	v_exp_f32_e32 v90, v90
	v_exp_f32_e32 v91, v91
	v_exp_f32_e32 v92, v92
	v_exp_f32_e32 v93, v93
	v_exp_f32_e32 v94, v94
	v_exp_f32_e32 v95, v95
	v_exp_f32_e32 v96, v96
	v_exp_f32_e32 v97, v97
	v_add_f32_e32 v126, v50, v82
	v_add_f32_e32 v127, v51, v83
	v_cvt_pk_bf16_f32 v50, v50, v51
	v_cvt_pk_bf16_f32 v51, v52, v53
	v_add_f32_e64 v210, v52, v84
	v_add_f32_e64 v211, v53, v85
	v_cvt_pk_bf16_f32 v52, v54, v55
	v_cvt_pk_bf16_f32 v53, v56, v57
	v_add_f32_e64 v126, v210, v126
	v_add_f32_e64 v127, v211, v127
	v_add_f32_e64 v210, v54, v86
	v_add_f32_e64 v211, v55, v87
	v_cvt_pk_bf16_f32 v54, v58, v59
	v_add_f32_e64 v126, v210, v126
	v_add_f32_e64 v127, v211, v127
	v_add_f32_e64 v210, v56, v88
	v_add_f32_e64 v211, v57, v89
	v_cvt_pk_bf16_f32 v55, v60, v61
	v_cvt_pk_bf16_f32 v56, v62, v63
	v_cvt_pk_bf16_f32 v57, v64, v65
	v_add_f32_e64 v126, v210, v126
	v_add_f32_e64 v127, v211, v127
	v_add_f32_e32 v210, v58, v90
	v_add_f32_e32 v211, v59, v91
	v_cvt_pk_bf16_f32 v58, v82, v83
	v_cvt_pk_bf16_f32 v59, v84, v85
	v_add_f32_e64 v126, v210, v126
	v_add_f32_e64 v127, v211, v127
	v_add_f32_e64 v210, v60, v92
	v_add_f32_e64 v211, v61, v93
	v_cvt_pk_bf16_f32 v60, v86, v87
	v_cvt_pk_bf16_f32 v61, v88, v89
	v_add_f32_e64 v126, v210, v126
	v_add_f32_e64 v127, v211, v127
	v_add_f32_e32 v210, v62, v94
	v_add_f32_e32 v211, v63, v95
	v_cvt_pk_bf16_f32 v62, v90, v91
	v_cvt_pk_bf16_f32 v63, v92, v93
	v_add_f32_e64 v126, v210, v126
	v_add_f32_e64 v127, v211, v127
	v_add_f32_e64 v210, v64, v96
	v_add_f32_e64 v211, v65, v97
	v_cvt_pk_bf16_f32 v64, v94, v95
	v_cvt_pk_bf16_f32 v65, v96, v97
	v_add_f32_e64 v126, v210, v126
	v_add_f32_e64 v127, v211, v127
	v_add_f32_e32 v126, v126, v127
	v_mov_b32_e32 v127, v126
	s_nop 1
	v_permlane32_swap_b32_e32 v126, v127
	s_andn2_b64 vcc, exec, s[14:15]
	s_mov_b64 s[6:7], -1
	s_cbranch_vccz .LBB0_710

; DEVI void pv_both(f32x16& o0, f32x16& o1, int vb, bf16x8 pa0, bf16x8 pa1, bf16x8 pa2, bf16x8 pa3) {
;     const s16x4 a0 = tr_read<v_rd_off(0, 0, 0)>(vb), b0 = tr_read<v_rd_off(0, 0, 1)>(vb), a1 = tr_read<v_rd_off(0, 1, 0)>(vb), b1 = tr_read<v_rd_off(0, 1, 1)>(vb);
;     const s16x4 a2 = tr_read<v_rd_off(0, 2, 0)>(vb), b2 = tr_read<v_rd_off(0, 2, 1)>(vb), a3 = tr_read<v_rd_off(0, 3, 0)>(vb), b3 = tr_read<v_rd_off(0, 3, 1)>(vb);
;     const s16x4 c0 = tr_read<v_rd_off(1, 0, 0)>(vb), d0 = tr_read<v_rd_off(1, 0, 1)>(vb), c1 = tr_read<v_rd_off(1, 1, 0)>(vb), d1 = tr_read<v_rd_off(1, 1, 1)>(vb);
;     const s16x4 c2 = tr_read<v_rd_off(1, 2, 0)>(vb), d2 = tr_read<v_rd_off(1, 2, 1)>(vb), c3 = tr_read<v_rd_off(1, 3, 0)>(vb), d3 = tr_read<v_rd_off(1, 3, 1)>(vb);
;     asm volatile("s_waitcnt lgkmcnt(8)" ::: "memory"); SBAR();
;     ...
;     o0 = __builtin_amdgcn_mfma_f32_32x32x16_bf16(pa0, PK(a0, b0), o0, 0, 0, 0);
;     o0 = __builtin_amdgcn_mfma_f32_32x32x16_bf16(pa1, PK(a1, b1), o0, 0, 0, 0);
;     o0 = __builtin_amdgcn_mfma_f32_32x32x16_bf16(pa2, PK(a2, b2), o0, 0, 0, 0);
;     o0 = __builtin_amdgcn_mfma_f32_32x32x16_bf16(pa3, PK(a3, b3), o0, 0, 0, 0);
;     asm volatile("s_waitcnt lgkmcnt(0)" ::: "memory"); SBAR();
;     o1 = __builtin_amdgcn_mfma_f32_32x32x16_bf16(pa0, PK(c0, d0), o1, 0, 0, 0);
;     o1 = __builtin_amdgcn_mfma_f32_32x32x16_bf16(pa1, PK(c1, d1), o1, 0, 0, 0);
;     o1 = __builtin_amdgcn_mfma_f32_32x32x16_bf16(pa2, PK(c2, d2), o1, 0, 0, 0);
;     o1 = __builtin_amdgcn_mfma_f32_32x32x16_bf16(pa3, PK(c3, d3), o1, 0, 0, 0);
;     ...
; }
; template <bool FIRST> DEVI bool partialSM(f32x16& p0, f32x16& p1, float& m_reg, float& alpha) {
;     float pmax = p0[0];
; #pragma unroll
;     for (int r = 1; r < 16; ++r) pmax = fmaxf(pmax, p0[r]);
; #pragma unroll
;     for (int r = 0; r < 16; ++r) pmax = fmaxf(pmax, p1[r]);
;     { auto rr = __builtin_amdgcn_permlane32_swap(__float_as_uint(pmax), __float_as_uint(pmax), false, false);
;       pmax = fmaxf(__uint_as_float(rr[0]), __uint_as_float(rr[1])); }
;     if (FIRST) { m_reg = pmax; alpha = 1.f;
; #pragma unroll
;         for (int r = 0; r < 16; ++r) { p0[r] = __builtin_amdgcn_exp2f(p0[r] - pmax); p1[r] = p1[r] - pmax; }
;         return false;
;     } else if (__builtin_expect(__all(pmax <= ATT_THR), 1)) { alpha = 1.f;
; #pragma unroll
;         for (int r = 0; r < 16; ++r) p0[r] = __builtin_amdgcn_exp2f(p0[r]);
.LBB0_702:
	s_mul_i32 s98, s2, 0x6000
	s_add_i32 s98, s96, s98
	s_lshl_b32 s99, s2, 14
	s_add_i32 s99, s97, s99
	s_mul_i32 s6, s61, 0x6000
	s_add_i32 s6, s6, 0
	v_add_u32_e32 v249, s6, v129
	v_lshl_add_u64 v[250:251], v[118:119], 0, s[12:13]
	s_mov_b32 m0, s98
	s_barrier
	ds_read_b128 v[234:237], v249
	ds_read_b128 v[210:213], v249 offset:6144
	global_load_lds_dwordx4 v[250:251], off
	s_waitcnt lgkmcnt(1)
	v_mfma_f32_32x32x16_bf16 v[98:113], v[234:237], v[150:153], v[34:49]
	v_add_u32_e32 v249, s6, v184
	v_lshl_add_u64 v[250:251], v[120:121], 0, s[12:13]
	s_add_i32 m0, s98, 0x2000
	global_load_lds_dwordx4 v[250:251], off
	s_waitcnt lgkmcnt(0)
	v_mfma_f32_32x32x16_bf16 v[66:81], v[210:213], v[150:153], v[34:49]
	ds_read_b128 v[210:213], v249
	ds_read_b128 v[214:217], v249 offset:6144
	v_add_u32_e32 v249, s6, v185
	v_lshl_add_u64 v[250:251], v[122:123], 0, s[12:13]
	s_add_i32 m0, s98, 0x4000
	global_load_lds_dwordx4 v[250:251], off
	s_waitcnt lgkmcnt(1)
	v_mfma_f32_32x32x16_bf16 v[98:113], v[210:213], v[138:141], v[98:113]
	s_mov_b32 m0, s99
	v_lshl_add_u64 v[250:251], v[116:117], 0, s[40:41]
	global_load_lds_dwordx4 v[116:117], off
	s_add_i32 m0, s99, 0x2000
	v_add_u32_e32 v174, 0x2000, v202
	global_load_lds_dwordx4 v[250:251], off
	s_waitcnt lgkmcnt(0)
	v_mfma_f32_32x32x16_bf16 v[66:81], v[214:217], v[138:141], v[66:81]
	ds_read_b128 v[210:213], v249
	ds_read_b128 v[214:217], v249 offset:6144
	v_add_u32_e32 v249, s6, v204
	s_waitcnt lgkmcnt(1)
	v_mfma_f32_32x32x16_bf16 v[98:113], v[210:213], v[134:137], v[98:113]
	ds_read_b128 v[210:213], v249
	ds_read_b128 v[218:221], v249 offset:6144
	v_add_u32_e32 v249, s6, v205
	s_waitcnt lgkmcnt(2)
	v_mfma_f32_32x32x16_bf16 v[66:81], v[214:217], v[134:137], v[66:81]
	ds_read_b128 v[214:217], v249
	ds_read_b128 v[222:225], v249 offset:6144
	v_add_u32_e32 v249, s6, v206
	ds_read_b128 v[226:229], v249
	ds_read_b128 v[230:233], v249 offset:6144
	s_waitcnt lgkmcnt(5)
	v_mfma_f32_32x32x16_bf16 v[98:113], v[210:213], v[130:133], v[98:113]
	s_waitcnt lgkmcnt(4)
	v_mfma_f32_32x32x16_bf16 v[66:81], v[218:221], v[130:133], v[66:81]
	s_waitcnt lgkmcnt(3)
	v_mfma_f32_32x32x16_bf16 v[98:113], v[214:217], v[146:149], v[98:113]
	s_waitcnt lgkmcnt(2)
	v_mfma_f32_32x32x16_bf16 v[66:81], v[222:225], v[146:149], v[66:81]
	ds_read_b64_tr_b16 v[154:155], v174 offset:0
	ds_read_b64_tr_b16 v[156:157], v174 offset:0x400
	ds_read_b64_tr_b16 v[158:159], v174 offset:0x800
	ds_read_b64_tr_b16 v[160:161], v174 offset:0xc00
	ds_read_b64_tr_b16 v[162:163], v174 offset:0x1000
	ds_read_b64_tr_b16 v[164:165], v174 offset:0x1400
	ds_read_b64_tr_b16 v[166:167], v174 offset:0x1800
	ds_read_b64_tr_b16 v[168:169], v174 offset:0x1c00
	ds_read_b64_tr_b16 v[210:211], v174 offset:0x200
	ds_read_b64_tr_b16 v[212:213], v174 offset:0x600
	ds_read_b64_tr_b16 v[214:215], v174 offset:0xa00
	s_waitcnt lgkmcnt(12)
	v_mfma_f32_32x32x16_bf16 v[98:113], v[226:229], v[142:145], v[98:113]
	ds_read_b64_tr_b16 v[216:217], v174 offset:0xe00
	ds_read_b64_tr_b16 v[218:219], v174 offset:0x1200
	ds_read_b64_tr_b16 v[220:221], v174 offset:0x1600
	ds_read_b64_tr_b16 v[222:223], v174 offset:0x1a00
	ds_read_b64_tr_b16 v[224:225], v174 offset:0x1e00
	s_waitcnt lgkmcnt(15)
	v_mfma_f32_32x32x16_bf16 v[66:81], v[230:233], v[142:145], v[66:81]
	s_waitcnt lgkmcnt(14)
	v_mfma_f32_32x32x16_bf16 v[18:33], v[50:53], v[154:157], v[18:33]
	s_waitcnt lgkmcnt(6)
	v_mfma_f32_32x32x16_bf16 v[2:17], v[50:53], v[210:213], v[2:17]
	s_nop 4
	v_max_f32_e32 v249, v99, v99
	v_max_f32_e32 v250, v98, v98
	v_max_f32_e32 v249, v250, v249
	v_max3_f32 v249, v249, v100, v101
	v_max3_f32 v249, v249, v102, v103
	v_max3_f32 v251, v249, v104, v105
	v_max3_f32 v251, v251, v106, v107
	v_exp_f32_e32 v50, v98
	v_exp_f32_e32 v51, v99
	v_exp_f32_e32 v52, v100
	v_exp_f32_e32 v53, v101
	v_mfma_f32_32x32x16_bf16 v[18:33], v[54:57], v[158:161], v[18:33]
	s_waitcnt lgkmcnt(4)
	v_mfma_f32_32x32x16_bf16 v[2:17], v[54:57], v[214:217], v[2:17]
	v_max3_f32 v251, v251, v108, v109
	v_max3_f32 v251, v251, v110, v111
	v_max3_f32 v251, v251, v112, v113
	v_max3_f32 v251, v251, v66, v67
	v_max3_f32 v251, v251, v68, v69
	v_max3_f32 v251, v251, v70, v71
	v_max3_f32 v251, v251, v72, v73
	v_exp_f32_e32 v54, v102
	v_exp_f32_e32 v55, v103
	v_exp_f32_e32 v56, v104
	v_exp_f32_e32 v57, v105
	v_mfma_f32_32x32x16_bf16 v[18:33], v[58:61], v[162:165], v[18:33]
	s_waitcnt lgkmcnt(2)
	v_mfma_f32_32x32x16_bf16 v[2:17], v[58:61], v[218:221], v[2:17]
	v_max3_f32 v251, v251, v74, v75
	v_max3_f32 v251, v251, v76, v77
	v_max3_f32 v251, v251, v78, v79
	v_max3_f32 v251, v251, v80, v81
	v_mov_b32_e32 v252, v251
	s_nop 1
	v_permlane32_swap_b32_e32 v251, v252
	v_exp_f32_e32 v58, v106
	v_exp_f32_e32 v59, v107
	v_exp_f32_e32 v60, v108
	v_exp_f32_e32 v61, v109
	v_mfma_f32_32x32x16_bf16 v[18:33], v[62:65], v[166:169], v[18:33]
	s_waitcnt lgkmcnt(0)
	v_mfma_f32_32x32x16_bf16 v[2:17], v[62:65], v[222:225], v[2:17]
	v_exp_f32_e32 v62, v110
	v_exp_f32_e32 v63, v111
	v_exp_f32_e32 v64, v112
	v_exp_f32_e32 v65, v113
	v_max_f32_e32 v252, v252, v252
	v_max_f32_e32 v251, v251, v251
	v_max_f32_e32 v174, v251, v252
	v_cmp_ge_f32_e32 vcc, s79, v174
	s_cmp_lg_u64 vcc, exec
	s_cselect_b64 s[6:7], -1, 0
	s_cbranch_scc1 .LBB0_711
	v_mov_b32_e32 v202, 1.0
	v_mov_b32_e32 v203, v209
	s_branch .LBB0_716

; #define LAS __attribute__((address_space(3)))
; DEVI int v_rd_base(int lane) { return ((lane & 3) << 3) | (((lane >> 2) & 3) << 6) | (((lane >> 4) & 1) << 5) | (((lane >> 5) & 1) << 8); }
; #define VM0() asm volatile("s_waitcnt vmcnt(0)" ::: "memory")
; DEVI void attn_unit8(const Params& p, char* smem, int unit, int l, int& cvs  , CvRun& crun) {
;     ...
;     const int vb0 = (int)(uintptr_t)(LAS char*)V_lds + v_rd_base(lane);
;     float m_reg = 0.f, l_reg = 0.f; f32x16 o[2];
; #pragma unroll
;     for (int d = 0; d < 2; ++d)
; #pragma unroll
;         for (int r = 0; r < 16; ++r) o[d][r] = 0.f;
;     f32x16 pA0, pA1, pB0, pB1; float alA, alB; bf16x8 pa0, pa1, pa2, pa3;
;     constexpr int NTILE = S_ / 128;
;     B_DMA(0, 0); B_DMA(1, 1); VM0(); __syncthreads();
;     f32x16 cinit;
.LBB0_707:
	s_and_saveexec_b64 s[6:7], s[4:5]
	ds_write_b32 v187, v208 offset:128
	s_or_b64 exec, exec, s[6:7]
	v_add_u32_e32 v46, s91, v178
	s_waitcnt lgkmcnt(0)
	ds_read_b128 v[34:37], v46 offset:224
	ds_read_b128 v[38:41], v46 offset:192
	ds_read_b128 v[42:45], v46 offset:160
	ds_read_b128 v[46:49], v46 offset:128
	s_waitcnt lgkmcnt(0)
	v_pk_mul_f32 v[30:31], v[30:31], v[34:35]
	v_pk_mul_f32 v[14:15], v[14:15], v[34:35]
	v_xor_b32_e32 v34, 0x80000000, v209
	s_waitcnt lgkmcnt(2)
	v_pk_mul_f32 v[26:27], v[26:27], v[38:39]
	s_waitcnt lgkmcnt(1)
	v_pk_mul_f32 v[22:23], v[22:23], v[42:43]
	v_pk_mul_f32 v[32:33], v[32:33], v[36:37]
	v_pk_mul_f32 v[28:29], v[28:29], v[40:41]
	v_pk_mul_f32 v[24:25], v[24:25], v[44:45]
	s_waitcnt lgkmcnt(0)
	v_pk_mul_f32 v[20:21], v[20:21], v[48:49]
	v_pk_mul_f32 v[18:19], v[18:19], v[46:47]
	v_pk_mul_f32 v[10:11], v[10:11], v[38:39]
	v_pk_mul_f32 v[6:7], v[6:7], v[42:43]
	v_pk_mul_f32 v[16:17], v[16:17], v[36:37]
	v_pk_mul_f32 v[12:13], v[12:13], v[40:41]
	v_pk_mul_f32 v[8:9], v[8:9], v[44:45]
	v_pk_mul_f32 v[4:5], v[4:5], v[48:49]
	v_pk_mul_f32 v[2:3], v[2:3], v[46:47]
	v_mov_b32_e32 v35, v34
	v_mov_b32_e32 v36, v34
	v_mov_b32_e32 v37, v34
	v_mov_b32_e32 v38, v34
	v_mov_b32_e32 v39, v34
	v_mov_b32_e32 v40, v34
	v_mov_b32_e32 v41, v34
	v_mov_b32_e32 v42, v34
	v_mov_b32_e32 v43, v34
	v_mov_b32_e32 v44, v34
	v_mov_b32_e32 v45, v34
	v_mov_b32_e32 v46, v34
	v_mov_b32_e32 v47, v34
	v_mov_b32_e32 v48, v34
	v_mov_b32_e32 v49, v34
	s_branch .LBB0_699

; #define PK4(P, BASE, OUT) do { u32x4 w = {cvt_pk_bf16(P[BASE + 0], P[BASE + 1]), cvt_pk_bf16(P[BASE + 2], P[BASE + 3]), cvt_pk_bf16(P[BASE + 4], P[BASE + 5]), cvt_pk_bf16(P[BASE + 6], P[BASE + 7])}; \
;     OUT = *reinterpret_cast<bf16x8*>(&w); } while (0)
; DEVI void finishSM(f32x16& p0, f32x16& p1, float alpha, float& l_reg, bf16x8& pa0, bf16x8& pa1, bf16x8& pa2, bf16x8& pa3) {
; #pragma unroll
;     for (int r = 0; r < 16; ++r) p1[r] = __builtin_amdgcn_exp2f(p1[r]);
;     f32x2 s2 = (f32x2){p0[0], p0[1]} + (f32x2){p1[0], p1[1]};
; #pragma unroll
;     for (int r = 2; r < 16; r += 2) s2 += (f32x2){p0[r], p0[r + 1]} + (f32x2){p1[r], p1[r + 1]};
;     float ps = s2[0] + s2[1];
;     { auto rr = __builtin_amdgcn_permlane32_swap(__float_as_uint(ps), __float_as_uint(ps), false, false);
;       ps = __uint_as_float(rr[0]) + __uint_as_float(rr[1]); }
;     l_reg = l_reg * alpha + ps;
;     ...
;     PK4(p0, 0, pa0); PK4(p0, 8, pa1); PK4(p1, 0, pa2); PK4(p1, 8, pa3);
;     ...
; }
.LBB0_2263:
	v_exp_f32_e32 v82, v82
	v_exp_f32_e32 v83, v83
	v_exp_f32_e32 v84, v84
	v_exp_f32_e32 v85, v85
	v_exp_f32_e32 v86, v86
	v_exp_f32_e32 v87, v87
	v_exp_f32_e32 v88, v88
	v_exp_f32_e32 v89, v89
	v_exp_f32_e32 v90, v90
	v_exp_f32_e32 v91, v91
	v_exp_f32_e32 v92, v92
	v_exp_f32_e32 v93, v93
	v_exp_f32_e32 v94, v94
	v_exp_f32_e32 v95, v95
	v_exp_f32_e32 v96, v96
	v_exp_f32_e32 v97, v97
	v_add_f32_e32 v126, v50, v82
	v_add_f32_e32 v127, v51, v83
	v_cvt_pk_bf16_f32 v50, v50, v51
	v_cvt_pk_bf16_f32 v51, v52, v53
	v_add_f32_e64 v212, v52, v84
	v_add_f32_e64 v213, v53, v85
	v_cvt_pk_bf16_f32 v52, v54, v55
	v_cvt_pk_bf16_f32 v53, v56, v57
	v_add_f32_e64 v126, v212, v126
	v_add_f32_e64 v127, v213, v127
	v_add_f32_e64 v212, v54, v86
	v_add_f32_e64 v213, v55, v87
	v_cvt_pk_bf16_f32 v54, v58, v59
	v_add_f32_e64 v126, v212, v126
	v_add_f32_e64 v127, v213, v127
	v_add_f32_e64 v212, v56, v88
	v_add_f32_e64 v213, v57, v89
	v_cvt_pk_bf16_f32 v55, v60, v61
	v_cvt_pk_bf16_f32 v56, v62, v63
	v_cvt_pk_bf16_f32 v57, v64, v65
	v_add_f32_e64 v126, v212, v126
	v_add_f32_e64 v127, v213, v127
	v_add_f32_e32 v212, v58, v90
	v_add_f32_e32 v213, v59, v91
	v_cvt_pk_bf16_f32 v58, v82, v83
	v_cvt_pk_bf16_f32 v59, v84, v85
	v_add_f32_e64 v126, v212, v126
	v_add_f32_e64 v127, v213, v127
	v_add_f32_e64 v212, v60, v92
	v_add_f32_e64 v213, v61, v93
	v_cvt_pk_bf16_f32 v60, v86, v87
	v_cvt_pk_bf16_f32 v61, v88, v89
	v_add_f32_e64 v126, v212, v126
	v_add_f32_e64 v127, v213, v127
	v_add_f32_e32 v212, v62, v94
	v_add_f32_e32 v213, v63, v95
	v_cvt_pk_bf16_f32 v62, v90, v91
	v_cvt_pk_bf16_f32 v63, v92, v93
	v_add_f32_e64 v126, v212, v126
	v_add_f32_e64 v127, v213, v127
	v_add_f32_e64 v212, v64, v96
	v_add_f32_e64 v213, v65, v97
	v_cvt_pk_bf16_f32 v64, v94, v95
	v_cvt_pk_bf16_f32 v65, v96, v97
	v_add_f32_e64 v126, v212, v126
	v_add_f32_e64 v127, v213, v127
	v_add_f32_e32 v126, v126, v127
	v_mov_b32_e32 v127, v126
	s_nop 1
	v_permlane32_swap_b32_e32 v126, v127
	s_andn2_b64 vcc, exec, s[14:15]
	s_mov_b64 s[6:7], -1
	s_cbranch_vccz .LBB0_2274

; DEVI void pv_both(f32x16& o0, f32x16& o1, int vb, bf16x8 pa0, bf16x8 pa1, bf16x8 pa2, bf16x8 pa3) {
;     const s16x4 a0 = tr_read<v_rd_off(0, 0, 0)>(vb), b0 = tr_read<v_rd_off(0, 0, 1)>(vb), a1 = tr_read<v_rd_off(0, 1, 0)>(vb), b1 = tr_read<v_rd_off(0, 1, 1)>(vb);
;     const s16x4 a2 = tr_read<v_rd_off(0, 2, 0)>(vb), b2 = tr_read<v_rd_off(0, 2, 1)>(vb), a3 = tr_read<v_rd_off(0, 3, 0)>(vb), b3 = tr_read<v_rd_off(0, 3, 1)>(vb);
;     const s16x4 c0 = tr_read<v_rd_off(1, 0, 0)>(vb), d0 = tr_read<v_rd_off(1, 0, 1)>(vb), c1 = tr_read<v_rd_off(1, 1, 0)>(vb), d1 = tr_read<v_rd_off(1, 1, 1)>(vb);
;     const s16x4 c2 = tr_read<v_rd_off(1, 2, 0)>(vb), d2 = tr_read<v_rd_off(1, 2, 1)>(vb), c3 = tr_read<v_rd_off(1, 3, 0)>(vb), d3 = tr_read<v_rd_off(1, 3, 1)>(vb);
;     asm volatile("s_waitcnt lgkmcnt(8)" ::: "memory"); SBAR();
;     ...
;     o0 = __builtin_amdgcn_mfma_f32_32x32x16_bf16(pa0, PK(a0, b0), o0, 0, 0, 0);
;     o0 = __builtin_amdgcn_mfma_f32_32x32x16_bf16(pa1, PK(a1, b1), o0, 0, 0, 0);
;     o0 = __builtin_amdgcn_mfma_f32_32x32x16_bf16(pa2, PK(a2, b2), o0, 0, 0, 0);
;     o0 = __builtin_amdgcn_mfma_f32_32x32x16_bf16(pa3, PK(a3, b3), o0, 0, 0, 0);
;     asm volatile("s_waitcnt lgkmcnt(0)" ::: "memory"); SBAR();
;     o1 = __builtin_amdgcn_mfma_f32_32x32x16_bf16(pa0, PK(c0, d0), o1, 0, 0, 0);
;     o1 = __builtin_amdgcn_mfma_f32_32x32x16_bf16(pa1, PK(c1, d1), o1, 0, 0, 0);
;     o1 = __builtin_amdgcn_mfma_f32_32x32x16_bf16(pa2, PK(c2, d2), o1, 0, 0, 0);
;     o1 = __builtin_amdgcn_mfma_f32_32x32x16_bf16(pa3, PK(c3, d3), o1, 0, 0, 0);
;     ...
; }
; template <bool FIRST> DEVI bool partialSM(f32x16& p0, f32x16& p1, float& m_reg, float& alpha) {
;     float pmax = p0[0];
; #pragma unroll
;     for (int r = 1; r < 16; ++r) pmax = fmaxf(pmax, p0[r]);
; #pragma unroll
;     for (int r = 0; r < 16; ++r) pmax = fmaxf(pmax, p1[r]);
;     { auto rr = __builtin_amdgcn_permlane32_swap(__float_as_uint(pmax), __float_as_uint(pmax), false, false);
;       pmax = fmaxf(__uint_as_float(rr[0]), __uint_as_float(rr[1])); }
;     if (FIRST) { m_reg = pmax; alpha = 1.f;
; #pragma unroll
;         for (int r = 0; r < 16; ++r) { p0[r] = __builtin_amdgcn_exp2f(p0[r] - pmax); p1[r] = p1[r] - pmax; }
;         return false;
;     } else if (__builtin_expect(__all(pmax <= ATT_THR), 1)) { alpha = 1.f;
; #pragma unroll
;         for (int r = 0; r < 16; ++r) p0[r] = __builtin_amdgcn_exp2f(p0[r]);
.LBB0_2266:
	s_mul_i32 s98, s61, 0x6000
	s_add_i32 s98, s96, s98
	s_lshl_b32 s99, s61, 14
	s_add_i32 s99, s97, s99
	s_mul_i32 s6, s2, 0x6000
	s_add_i32 s6, s6, 0
	v_add_u32_e32 v249, s6, v129
	v_lshl_add_u64 v[250:251], v[118:119], 0, s[12:13]
	s_mov_b32 m0, s98
	s_barrier
	ds_read_b128 v[234:237], v249
	ds_read_b128 v[212:215], v249 offset:6144
	global_load_lds_dwordx4 v[250:251], off
	s_waitcnt lgkmcnt(1)
	v_mfma_f32_32x32x16_bf16 v[98:113], v[234:237], v[150:153], v[34:49]
	v_add_u32_e32 v249, s6, v184
	v_lshl_add_u64 v[250:251], v[120:121], 0, s[12:13]
	s_add_i32 m0, s98, 0x2000
	global_load_lds_dwordx4 v[250:251], off
	s_waitcnt lgkmcnt(0)
	v_mfma_f32_32x32x16_bf16 v[66:81], v[212:215], v[150:153], v[34:49]
	ds_read_b128 v[212:215], v249
	ds_read_b128 v[216:219], v249 offset:6144
	v_add_u32_e32 v249, s6, v185
	v_lshl_add_u64 v[250:251], v[122:123], 0, s[12:13]
	s_add_i32 m0, s98, 0x4000
	global_load_lds_dwordx4 v[250:251], off
	s_waitcnt lgkmcnt(1)
	v_mfma_f32_32x32x16_bf16 v[98:113], v[212:215], v[138:141], v[98:113]
	s_mov_b32 m0, s99
	v_lshl_add_u64 v[250:251], v[116:117], 0, s[40:41]
	global_load_lds_dwordx4 v[116:117], off
	s_add_i32 m0, s99, 0x2000
	v_add_u32_e32 v174, 0x2000, v203
	global_load_lds_dwordx4 v[250:251], off
	s_waitcnt lgkmcnt(0)
	v_mfma_f32_32x32x16_bf16 v[66:81], v[216:219], v[138:141], v[66:81]
	ds_read_b128 v[212:215], v249
	ds_read_b128 v[216:219], v249 offset:6144
	v_add_u32_e32 v249, s6, v205
	s_waitcnt lgkmcnt(1)
	v_mfma_f32_32x32x16_bf16 v[98:113], v[212:215], v[134:137], v[98:113]
	ds_read_b128 v[212:215], v249
	ds_read_b128 v[220:223], v249 offset:6144
	v_add_u32_e32 v249, s6, v206
	s_waitcnt lgkmcnt(2)
	v_mfma_f32_32x32x16_bf16 v[66:81], v[216:219], v[134:137], v[66:81]
	ds_read_b128 v[216:219], v249
	ds_read_b128 v[224:227], v249 offset:6144
	v_add_u32_e32 v249, s6, v207
	ds_read_b128 v[228:231], v249
	ds_read_b128 v[232:235], v249 offset:6144
	s_waitcnt lgkmcnt(5)
	v_mfma_f32_32x32x16_bf16 v[98:113], v[212:215], v[130:133], v[98:113]
	s_waitcnt lgkmcnt(4)
	v_mfma_f32_32x32x16_bf16 v[66:81], v[220:223], v[130:133], v[66:81]
	s_waitcnt lgkmcnt(3)
	v_mfma_f32_32x32x16_bf16 v[98:113], v[216:219], v[146:149], v[98:113]
	s_waitcnt lgkmcnt(2)
	v_mfma_f32_32x32x16_bf16 v[66:81], v[224:227], v[146:149], v[66:81]
	ds_read_b64_tr_b16 v[154:155], v174 offset:0
	ds_read_b64_tr_b16 v[156:157], v174 offset:0x400
	ds_read_b64_tr_b16 v[158:159], v174 offset:0x800
	ds_read_b64_tr_b16 v[160:161], v174 offset:0xc00
	ds_read_b64_tr_b16 v[162:163], v174 offset:0x1000
	ds_read_b64_tr_b16 v[164:165], v174 offset:0x1400
	ds_read_b64_tr_b16 v[166:167], v174 offset:0x1800
	ds_read_b64_tr_b16 v[168:169], v174 offset:0x1c00
	ds_read_b64_tr_b16 v[212:213], v174 offset:0x200
	ds_read_b64_tr_b16 v[214:215], v174 offset:0x600
	ds_read_b64_tr_b16 v[216:217], v174 offset:0xa00
	s_waitcnt lgkmcnt(12)
	v_mfma_f32_32x32x16_bf16 v[98:113], v[228:231], v[142:145], v[98:113]
	ds_read_b64_tr_b16 v[218:219], v174 offset:0xe00
	ds_read_b64_tr_b16 v[220:221], v174 offset:0x1200
	ds_read_b64_tr_b16 v[222:223], v174 offset:0x1600
	ds_read_b64_tr_b16 v[224:225], v174 offset:0x1a00
	ds_read_b64_tr_b16 v[226:227], v174 offset:0x1e00
	s_waitcnt lgkmcnt(15)
	v_mfma_f32_32x32x16_bf16 v[66:81], v[232:235], v[142:145], v[66:81]
	s_waitcnt lgkmcnt(14)
	v_mfma_f32_32x32x16_bf16 v[18:33], v[50:53], v[154:157], v[18:33]
	s_waitcnt lgkmcnt(6)
	v_mfma_f32_32x32x16_bf16 v[2:17], v[50:53], v[212:215], v[2:17]
	s_nop 4
	v_max_f32_e32 v249, v99, v99
	v_max_f32_e32 v250, v98, v98
	v_max_f32_e32 v249, v250, v249
	v_max3_f32 v249, v249, v100, v101
	v_max3_f32 v249, v249, v102, v103
	v_max3_f32 v251, v249, v104, v105
	v_max3_f32 v251, v251, v106, v107
	v_exp_f32_e32 v50, v98
	v_exp_f32_e32 v51, v99
	v_exp_f32_e32 v52, v100
	v_exp_f32_e32 v53, v101
	v_mfma_f32_32x32x16_bf16 v[18:33], v[54:57], v[158:161], v[18:33]
	s_waitcnt lgkmcnt(4)
	v_mfma_f32_32x32x16_bf16 v[2:17], v[54:57], v[216:219], v[2:17]
	v_max3_f32 v251, v251, v108, v109
	v_max3_f32 v251, v251, v110, v111
	v_max3_f32 v251, v251, v112, v113
	v_max3_f32 v251, v251, v66, v67
	v_max3_f32 v251, v251, v68, v69
	v_max3_f32 v251, v251, v70, v71
	v_max3_f32 v251, v251, v72, v73
	v_exp_f32_e32 v54, v102
	v_exp_f32_e32 v55, v103
	v_exp_f32_e32 v56, v104
	v_exp_f32_e32 v57, v105
	v_mfma_f32_32x32x16_bf16 v[18:33], v[58:61], v[162:165], v[18:33]
	s_waitcnt lgkmcnt(2)
	v_mfma_f32_32x32x16_bf16 v[2:17], v[58:61], v[220:223], v[2:17]
	v_max3_f32 v251, v251, v74, v75
	v_max3_f32 v251, v251, v76, v77
	v_max3_f32 v251, v251, v78, v79
	v_max3_f32 v251, v251, v80, v81
	v_mov_b32_e32 v252, v251
	s_nop 1
	v_permlane32_swap_b32_e32 v251, v252
	v_exp_f32_e32 v58, v106
	v_exp_f32_e32 v59, v107
	v_exp_f32_e32 v60, v108
	v_exp_f32_e32 v61, v109
	v_mfma_f32_32x32x16_bf16 v[18:33], v[62:65], v[166:169], v[18:33]
	s_waitcnt lgkmcnt(0)
	v_mfma_f32_32x32x16_bf16 v[2:17], v[62:65], v[224:227], v[2:17]
	v_exp_f32_e32 v62, v110
	v_exp_f32_e32 v63, v111
	v_exp_f32_e32 v64, v112
	v_exp_f32_e32 v65, v113
	v_max_f32_e32 v252, v252, v252
	v_max_f32_e32 v251, v251, v251
	v_max_f32_e32 v174, v251, v252
	v_cmp_ge_f32_e32 vcc, s80, v174
	s_cmp_lg_u64 vcc, exec
	s_cselect_b64 s[6:7], -1, 0
	s_cbranch_scc1 .LBB0_2275
	v_mov_b32_e32 v203, 1.0
	v_mov_b32_e32 v204, v210
	s_branch .LBB0_2280

; #define LAS __attribute__((address_space(3)))
; DEVI int v_rd_base(int lane) { return ((lane & 3) << 3) | (((lane >> 2) & 3) << 6) | (((lane >> 4) & 1) << 5) | (((lane >> 5) & 1) << 8); }
; #define VM0() asm volatile("s_waitcnt vmcnt(0)" ::: "memory")
; DEVI void attn_unit8(const Params& p, char* smem, int unit, int l, int& cvs  , CvRun& crun) {
;     ...
;     const int vb0 = (int)(uintptr_t)(LAS char*)V_lds + v_rd_base(lane);
;     float m_reg = 0.f, l_reg = 0.f; f32x16 o[2];
; #pragma unroll
;     for (int d = 0; d < 2; ++d)
; #pragma unroll
;         for (int r = 0; r < 16; ++r) o[d][r] = 0.f;
;     f32x16 pA0, pA1, pB0, pB1; float alA, alB; bf16x8 pa0, pa1, pa2, pa3;
;     constexpr int NTILE = S_ / 128;
;     B_DMA(0, 0); B_DMA(1, 1); VM0(); __syncthreads();
;     f32x16 cinit;
.LBB0_2271:
	s_and_saveexec_b64 s[6:7], s[4:5]
	ds_write_b32 v188, v209 offset:128
	s_or_b64 exec, exec, s[6:7]
	v_add_u32_e32 v46, s93, v178
	s_waitcnt lgkmcnt(0)
	ds_read_b128 v[34:37], v46 offset:224
	ds_read_b128 v[38:41], v46 offset:192
	ds_read_b128 v[42:45], v46 offset:160
	ds_read_b128 v[46:49], v46 offset:128
	s_waitcnt lgkmcnt(0)
	v_pk_mul_f32 v[30:31], v[30:31], v[34:35]
	v_pk_mul_f32 v[14:15], v[14:15], v[34:35]
	v_xor_b32_e32 v34, 0x80000000, v210
	s_waitcnt lgkmcnt(2)
	v_pk_mul_f32 v[26:27], v[26:27], v[38:39]
	s_waitcnt lgkmcnt(1)
	v_pk_mul_f32 v[22:23], v[22:23], v[42:43]
	v_pk_mul_f32 v[32:33], v[32:33], v[36:37]
	v_pk_mul_f32 v[28:29], v[28:29], v[40:41]
	v_pk_mul_f32 v[24:25], v[24:25], v[44:45]
	s_waitcnt lgkmcnt(0)
	v_pk_mul_f32 v[20:21], v[20:21], v[48:49]
	v_pk_mul_f32 v[18:19], v[18:19], v[46:47]
	v_pk_mul_f32 v[10:11], v[10:11], v[38:39]
	v_pk_mul_f32 v[6:7], v[6:7], v[42:43]
	v_pk_mul_f32 v[16:17], v[16:17], v[36:37]
	v_pk_mul_f32 v[12:13], v[12:13], v[40:41]
	v_pk_mul_f32 v[8:9], v[8:9], v[44:45]
	v_pk_mul_f32 v[4:5], v[4:5], v[48:49]
	v_pk_mul_f32 v[2:3], v[2:3], v[46:47]
	v_mov_b32_e32 v35, v34
	v_mov_b32_e32 v36, v34
	v_mov_b32_e32 v37, v34
	v_mov_b32_e32 v38, v34
	v_mov_b32_e32 v39, v34
	v_mov_b32_e32 v40, v34
	v_mov_b32_e32 v41, v34
	v_mov_b32_e32 v42, v34
	v_mov_b32_e32 v43, v34
	v_mov_b32_e32 v44, v34
	v_mov_b32_e32 v45, v34
	v_mov_b32_e32 v46, v34
	v_mov_b32_e32 v47, v34
	v_mov_b32_e32 v48, v34
	v_mov_b32_e32 v49, v34
	s_branch .LBB0_2263
